# grid barrier: L1 invalidate issued right behind the arrival atomic by every WG (atomic waited alone with vmcnt(1)); later copies dropped
# baseline (speedup 1.0000x reference)
; __device__ __forceinline__ unsigned xb_ld(unsigned* p)              { return __hip_atomic_load(p, __ATOMIC_RELAXED, __HIP_MEMORY_SCOPE_AGENT); }
; __device__ __forceinline__ unsigned xb_add(unsigned* p, unsigned v) { return __hip_atomic_fetch_add(p, v, __ATOMIC_RELAXED, __HIP_MEMORY_SCOPE_AGENT); }
; #define XB_SPIN(cond, bar) do { unsigned _sp = 0; while (cond) { __builtin_amdgcn_s_sleep(1); \
;     if ((++_sp & 255u) == 0u) { if (xb_ld(&(bar)[XB_TMO])) break; if (_sp > XB_SPIN_CAP) { atomicAdd(&(bar)[XB_TMO], 1u); break; } } } } while (0)
; __device__ __forceinline__ void xcd_barrier(const XcdBarrier& b) {
;     ...
;         unsigned nloc = b.st[0], nx = b.st[1];
;         if (nloc == 0u) { xcd_barrier_complete(bar, b.x, nloc, nx); b.st[0] = nloc; b.st[1] = nx; }
;         const unsigned old = xb_add(&bar[XB_XSUB(b.x)], 1u);
;         const unsigned gen = old / nloc;
;         if (old + 1u == (gen + 1u) * nloc) {
;             __builtin_amdgcn_fence(__ATOMIC_RELEASE, "agent");
;             asm volatile("s_waitcnt vmcnt(0)" ::: "memory");
;             const unsigned og = xb_add(&bar[XB_TOP], 1u);
;             const unsigned tg = og / nx;
;             if (og + 1u == (tg + 1u) * nx) xb_add(&bar[XB_TOPGEN], 1u);
;             else XB_SPIN(xb_ld(&bar[XB_TOPGEN]) == tg, bar);
;             __builtin_amdgcn_fence(__ATOMIC_ACQUIRE, "agent");
;             xb_add(&bar[XB_XGEN(b.x)], 1u);
;             asm volatile("s_waitcnt vmcnt(0)" ::: "memory");
;         } else {
;             XB_SPIN(xb_ld(&bar[XB_XGEN(b.x)]) == gen, bar);
;             __builtin_amdgcn_fence(__ATOMIC_ACQUIRE, "agent");
;             asm volatile("s_waitcnt vmcnt(0)" ::: "memory");
.LBB0_65:
	v_readlane_b32 s2, v253, 6
	s_lshl_b32 s2, s2, 8
	v_readlane_b32 s4, v253, 4
	v_readlane_b32 s5, v253, 5
	s_add_u32 s2, s4, s2
	s_addc_u32 s3, s5, 0
	v_mov_b32_e32 v2, 0x1000
	v_mov_b32_e32 v4, 1
	global_atomic_add v4, v2, v4, s[2:3] offset:1024 sc0
	buffer_inv sc1
	v_cvt_f32_u32_e32 v2, v3
	v_sub_u32_e32 v5, 0, v3
	v_rcp_iflag_f32_e32 v2, v2
	s_nop 0
	v_mul_f32_e32 v2, 0x4f7ffffe, v2
	v_cvt_u32_f32_e32 v2, v2
	v_mul_lo_u32 v5, v5, v2
	v_mul_hi_u32 v5, v2, v5
	v_add_u32_e32 v2, v2, v5
	s_waitcnt vmcnt(1)
	v_mul_hi_u32 v2, v4, v2
	v_mul_lo_u32 v5, v2, v3
	v_sub_u32_e32 v5, v4, v5
	v_add_u32_e32 v6, 1, v2
	v_cmp_ge_u32_e32 vcc, v5, v3
	v_add_u32_e32 v4, 1, v4
	s_nop 0
	v_cndmask_b32_e32 v2, v2, v6, vcc
	v_sub_u32_e32 v6, v5, v3
	v_cndmask_b32_e32 v5, v5, v6, vcc
	v_add_u32_e32 v6, 1, v2
	v_cmp_ge_u32_e32 vcc, v5, v3
	s_nop 1
	v_cndmask_b32_e32 v2, v2, v6, vcc
	v_mul_lo_u32 v5, v3, v2
	v_add_u32_e32 v3, v5, v3
	v_cmp_ne_u32_e32 vcc, v4, v3
	s_and_saveexec_b64 s[4:5], vcc
	s_xor_b64 s[4:5], exec, s[4:5]
	s_cbranch_execz .LBB0_79
	s_waitcnt lgkmcnt(0)
	v_mov_b32_e32 v1, 0x2000
	global_load_dword v1, v1, s[2:3] offset:1024 sc1
	s_add_u32 s10, s2, 0x2400
	s_addc_u32 s11, s3, 0
	s_waitcnt vmcnt(0)
	v_cmp_eq_u32_e32 vcc, v1, v2
	s_and_saveexec_b64 s[6:7], vcc
	s_cbranch_execz .LBB0_78
	s_add_u32 s8, s94, 0x4200
	s_addc_u32 s9, s95, 0
	s_mov_b32 s22, 1
	s_mov_b64 s[12:13], 0
	v_mov_b32_e32 v1, 0
	s_branch .LBB0_69

; __device__ __forceinline__ unsigned xb_ld(unsigned* p)              { return __hip_atomic_load(p, __ATOMIC_RELAXED, __HIP_MEMORY_SCOPE_AGENT); }
; __device__ __forceinline__ unsigned xb_add(unsigned* p, unsigned v) { return __hip_atomic_fetch_add(p, v, __ATOMIC_RELAXED, __HIP_MEMORY_SCOPE_AGENT); }
; #define XB_SPIN(cond, bar) do { unsigned _sp = 0; while (cond) { __builtin_amdgcn_s_sleep(1); \
;     if ((++_sp & 255u) == 0u) { if (xb_ld(&(bar)[XB_TMO])) break; if (_sp > XB_SPIN_CAP) { atomicAdd(&(bar)[XB_TMO], 1u); break; } } } } while (0)
; __device__ __forceinline__ void xcd_barrier(const XcdBarrier& b) {
;     ...
;         unsigned nloc = b.st[0], nx = b.st[1];
;         if (nloc == 0u) { xcd_barrier_complete(bar, b.x, nloc, nx); b.st[0] = nloc; b.st[1] = nx; }
;         const unsigned old = xb_add(&bar[XB_XSUB(b.x)], 1u);
;         const unsigned gen = old / nloc;
;         if (old + 1u == (gen + 1u) * nloc) {
;             __builtin_amdgcn_fence(__ATOMIC_RELEASE, "agent");
;             asm volatile("s_waitcnt vmcnt(0)" ::: "memory");
;             const unsigned og = xb_add(&bar[XB_TOP], 1u);
;             const unsigned tg = og / nx;
;             if (og + 1u == (tg + 1u) * nx) xb_add(&bar[XB_TOPGEN], 1u);
;             else XB_SPIN(xb_ld(&bar[XB_TOPGEN]) == tg, bar);
;             __builtin_amdgcn_fence(__ATOMIC_ACQUIRE, "agent");
;             xb_add(&bar[XB_XGEN(b.x)], 1u);
;             asm volatile("s_waitcnt vmcnt(0)" ::: "memory");
;         } else {
;             XB_SPIN(xb_ld(&bar[XB_XGEN(b.x)]) == gen, bar);
;             __builtin_amdgcn_fence(__ATOMIC_ACQUIRE, "agent");
;             asm volatile("s_waitcnt vmcnt(0)" ::: "memory");
.LBB0_226:
	v_readlane_b32 s2, v253, 6
	s_lshl_b32 s2, s2, 8
	v_readlane_b32 s4, v253, 4
	v_readlane_b32 s5, v253, 5
	s_add_u32 s2, s4, s2
	s_addc_u32 s3, s5, 0
	v_mov_b32_e32 v3, 0x1000
	v_mov_b32_e32 v5, 1
	global_atomic_add v5, v3, v5, s[2:3] offset:1024 sc0
	buffer_inv sc1
	v_cvt_f32_u32_e32 v3, v4
	v_sub_u32_e32 v6, 0, v4
	v_rcp_iflag_f32_e32 v3, v3
	s_nop 0
	v_mul_f32_e32 v3, 0x4f7ffffe, v3
	v_cvt_u32_f32_e32 v3, v3
	v_mul_lo_u32 v6, v6, v3
	v_mul_hi_u32 v6, v3, v6
	v_add_u32_e32 v3, v3, v6
	s_waitcnt vmcnt(1)
	v_mul_hi_u32 v3, v5, v3
	v_mul_lo_u32 v6, v3, v4
	v_sub_u32_e32 v6, v5, v6
	v_add_u32_e32 v7, 1, v3
	v_cmp_ge_u32_e32 vcc, v6, v4
	v_add_u32_e32 v5, 1, v5
	s_nop 0
	v_cndmask_b32_e32 v3, v3, v7, vcc
	v_sub_u32_e32 v7, v6, v4
	v_cndmask_b32_e32 v6, v6, v7, vcc
	v_add_u32_e32 v7, 1, v3
	v_cmp_ge_u32_e32 vcc, v6, v4
	s_nop 1
	v_cndmask_b32_e32 v3, v3, v7, vcc
	v_mul_lo_u32 v6, v4, v3
	v_add_u32_e32 v4, v6, v4
	v_cmp_ne_u32_e32 vcc, v5, v4
	s_and_saveexec_b64 s[4:5], vcc
	s_xor_b64 s[4:5], exec, s[4:5]
	s_cbranch_execz .LBB0_240
	s_waitcnt lgkmcnt(0)
	v_mov_b32_e32 v2, 0x2000
	global_load_dword v2, v2, s[2:3] offset:1024 sc1
	s_add_u32 s10, s2, 0x2400
	s_addc_u32 s11, s3, 0
	s_waitcnt vmcnt(0)
	v_cmp_eq_u32_e32 vcc, v2, v3
	s_and_saveexec_b64 s[6:7], vcc
	s_cbranch_execz .LBB0_239
	s_add_u32 s8, s94, 0x4200
	s_addc_u32 s9, s95, 0
	s_mov_b32 s22, 1
	s_mov_b64 s[12:13], 0
	v_mov_b32_e32 v2, 0
	s_branch .LBB0_230

; __device__ __forceinline__ unsigned xb_ld(unsigned* p)              { return __hip_atomic_load(p, __ATOMIC_RELAXED, __HIP_MEMORY_SCOPE_AGENT); }
; __device__ __forceinline__ unsigned xb_add(unsigned* p, unsigned v) { return __hip_atomic_fetch_add(p, v, __ATOMIC_RELAXED, __HIP_MEMORY_SCOPE_AGENT); }
; #define XB_SPIN(cond, bar) do { unsigned _sp = 0; while (cond) { __builtin_amdgcn_s_sleep(1); \
;     if ((++_sp & 255u) == 0u) { if (xb_ld(&(bar)[XB_TMO])) break; if (_sp > XB_SPIN_CAP) { atomicAdd(&(bar)[XB_TMO], 1u); break; } } } } while (0)
; __device__ __forceinline__ void xcd_barrier(const XcdBarrier& b) {
;     ...
;         unsigned nloc = b.st[0], nx = b.st[1];
;         if (nloc == 0u) { xcd_barrier_complete(bar, b.x, nloc, nx); b.st[0] = nloc; b.st[1] = nx; }
;         const unsigned old = xb_add(&bar[XB_XSUB(b.x)], 1u);
;         const unsigned gen = old / nloc;
;         if (old + 1u == (gen + 1u) * nloc) {
;             __builtin_amdgcn_fence(__ATOMIC_RELEASE, "agent");
;             asm volatile("s_waitcnt vmcnt(0)" ::: "memory");
;             const unsigned og = xb_add(&bar[XB_TOP], 1u);
;             const unsigned tg = og / nx;
;             if (og + 1u == (tg + 1u) * nx) xb_add(&bar[XB_TOPGEN], 1u);
;             else XB_SPIN(xb_ld(&bar[XB_TOPGEN]) == tg, bar);
;             __builtin_amdgcn_fence(__ATOMIC_ACQUIRE, "agent");
;             xb_add(&bar[XB_XGEN(b.x)], 1u);
;             asm volatile("s_waitcnt vmcnt(0)" ::: "memory");
;         } else {
;             XB_SPIN(xb_ld(&bar[XB_XGEN(b.x)]) == gen, bar);
;             __builtin_amdgcn_fence(__ATOMIC_ACQUIRE, "agent");
;             asm volatile("s_waitcnt vmcnt(0)" ::: "memory");
.LBB0_2295:
	v_readlane_b32 s12, v255, 7
	v_readlane_b32 s13, v255, 8
	v_cvt_f32_u32_e32 v3, v4
	v_sub_u32_e32 v6, 0, v4
	v_rcp_iflag_f32_e32 v3, v3
	s_nop 1
	global_atomic_add v5, v133, v171, s[12:13] sc0
	buffer_inv sc1
	v_mul_f32_e32 v3, 0x4f7ffffe, v3
	v_cvt_u32_f32_e32 v3, v3
	v_mul_lo_u32 v6, v6, v3
	v_mul_hi_u32 v6, v3, v6
	v_add_u32_e32 v3, v3, v6
	s_waitcnt vmcnt(1)
	v_mul_hi_u32 v3, v5, v3
	v_mul_lo_u32 v6, v3, v4
	v_sub_u32_e32 v6, v5, v6
	v_add_u32_e32 v7, 1, v3
	v_cmp_ge_u32_e32 vcc, v6, v4
	v_add_u32_e32 v5, 1, v5
	s_nop 0
	v_cndmask_b32_e32 v3, v3, v7, vcc
	v_sub_u32_e32 v7, v6, v4
	v_cndmask_b32_e32 v6, v6, v7, vcc
	v_add_u32_e32 v7, 1, v3
	v_cmp_ge_u32_e32 vcc, v6, v4
	s_nop 1
	v_cndmask_b32_e32 v3, v3, v7, vcc
	v_mul_lo_u32 v6, v4, v3
	v_add_u32_e32 v4, v6, v4
	v_cmp_ne_u32_e32 vcc, v5, v4
	s_and_saveexec_b64 s[12:13], vcc
	s_xor_b64 s[42:43], exec, s[12:13]
	s_cbranch_execz .LBB0_2309
	v_readlane_b32 s12, v254, 13
	v_readlane_b32 s13, v254, 14
	s_waitcnt lgkmcnt(0)
	s_nop 3
	global_load_dword v2, v133, s[12:13] sc1
	s_waitcnt vmcnt(0)
	v_cmp_eq_u32_e32 vcc, v2, v3
	s_and_saveexec_b64 s[46:47], vcc
	s_cbranch_execz .LBB0_2308
	s_mov_b32 s2, 1
	s_mov_b64 s[66:67], 0
	s_branch .LBB0_2299

; __device__ __forceinline__ unsigned xb_ld(unsigned* p)              { return __hip_atomic_load(p, __ATOMIC_RELAXED, __HIP_MEMORY_SCOPE_AGENT); }
; __device__ __forceinline__ unsigned xb_add(unsigned* p, unsigned v) { return __hip_atomic_fetch_add(p, v, __ATOMIC_RELAXED, __HIP_MEMORY_SCOPE_AGENT); }
; #define XB_SPIN(cond, bar) do { unsigned _sp = 0; while (cond) { __builtin_amdgcn_s_sleep(1); \
;     if ((++_sp & 255u) == 0u) { if (xb_ld(&(bar)[XB_TMO])) break; if (_sp > XB_SPIN_CAP) { atomicAdd(&(bar)[XB_TMO], 1u); break; } } } } while (0)
; __device__ __forceinline__ void xcd_barrier(const XcdBarrier& b) {
;     ...
;         unsigned nloc = b.st[0], nx = b.st[1];
;         if (nloc == 0u) { xcd_barrier_complete(bar, b.x, nloc, nx); b.st[0] = nloc; b.st[1] = nx; }
;         const unsigned old = xb_add(&bar[XB_XSUB(b.x)], 1u);
;         const unsigned gen = old / nloc;
;         if (old + 1u == (gen + 1u) * nloc) {
;             __builtin_amdgcn_fence(__ATOMIC_RELEASE, "agent");
;             asm volatile("s_waitcnt vmcnt(0)" ::: "memory");
;             const unsigned og = xb_add(&bar[XB_TOP], 1u);
;             const unsigned tg = og / nx;
;             if (og + 1u == (tg + 1u) * nx) xb_add(&bar[XB_TOPGEN], 1u);
;             else XB_SPIN(xb_ld(&bar[XB_TOPGEN]) == tg, bar);
;             __builtin_amdgcn_fence(__ATOMIC_ACQUIRE, "agent");
;             xb_add(&bar[XB_XGEN(b.x)], 1u);
;             asm volatile("s_waitcnt vmcnt(0)" ::: "memory");
;         } else {
;             XB_SPIN(xb_ld(&bar[XB_XGEN(b.x)]) == gen, bar);
;             __builtin_amdgcn_fence(__ATOMIC_ACQUIRE, "agent");
;             asm volatile("s_waitcnt vmcnt(0)" ::: "memory");
.LBB0_4431:
	v_readlane_b32 s0, v253, 6
	s_lshl_b32 s0, s0, 8
	v_readlane_b32 s4, v253, 4
	v_readlane_b32 s5, v253, 5
	s_add_u32 s0, s4, s0
	s_addc_u32 s1, s5, 0
	v_mov_b32_e32 v2, 0x1000
	v_mov_b32_e32 v4, 1
	global_atomic_add v4, v2, v4, s[0:1] offset:1024 sc0
	buffer_inv sc1
	v_cvt_f32_u32_e32 v2, v3
	v_sub_u32_e32 v5, 0, v3
	v_rcp_iflag_f32_e32 v2, v2
	s_nop 0
	v_mul_f32_e32 v2, 0x4f7ffffe, v2
	v_cvt_u32_f32_e32 v2, v2
	v_mul_lo_u32 v5, v5, v2
	v_mul_hi_u32 v5, v2, v5
	v_add_u32_e32 v2, v2, v5
	s_waitcnt vmcnt(1)
	v_mul_hi_u32 v2, v4, v2
	v_mul_lo_u32 v5, v2, v3
	v_sub_u32_e32 v5, v4, v5
	v_add_u32_e32 v6, 1, v2
	v_cmp_ge_u32_e32 vcc, v5, v3
	v_add_u32_e32 v4, 1, v4
	s_nop 0
	v_cndmask_b32_e32 v2, v2, v6, vcc
	v_sub_u32_e32 v6, v5, v3
	v_cndmask_b32_e32 v5, v5, v6, vcc
	v_add_u32_e32 v6, 1, v2
	v_cmp_ge_u32_e32 vcc, v5, v3
	s_nop 1
	v_cndmask_b32_e32 v2, v2, v6, vcc
	v_mul_lo_u32 v5, v3, v2
	v_add_u32_e32 v3, v5, v3
	v_cmp_ne_u32_e32 vcc, v4, v3
	s_and_saveexec_b64 s[4:5], vcc
	s_xor_b64 s[4:5], exec, s[4:5]
	s_cbranch_execz .LBB0_4445
	s_waitcnt lgkmcnt(0)
	v_mov_b32_e32 v1, 0x2000
	global_load_dword v1, v1, s[0:1] offset:1024 sc1
	s_add_u32 s10, s0, 0x2400
	s_addc_u32 s11, s1, 0
	s_waitcnt vmcnt(0)
	v_cmp_eq_u32_e32 vcc, v1, v2
	s_and_saveexec_b64 s[6:7], vcc
	s_cbranch_execz .LBB0_4444
	s_add_u32 s8, s94, 0x4200
	s_addc_u32 s9, s95, 0
	s_mov_b32 s22, 1
	s_mov_b64 s[12:13], 0
	v_mov_b32_e32 v1, 0
	s_branch .LBB0_4435

; __device__ __forceinline__ unsigned xb_ld(unsigned* p)              { return __hip_atomic_load(p, __ATOMIC_RELAXED, __HIP_MEMORY_SCOPE_AGENT); }
; __device__ __forceinline__ unsigned xb_add(unsigned* p, unsigned v) { return __hip_atomic_fetch_add(p, v, __ATOMIC_RELAXED, __HIP_MEMORY_SCOPE_AGENT); }
; #define XB_SPIN(cond, bar) do { unsigned _sp = 0; while (cond) { __builtin_amdgcn_s_sleep(1); \
;     if ((++_sp & 255u) == 0u) { if (xb_ld(&(bar)[XB_TMO])) break; if (_sp > XB_SPIN_CAP) { atomicAdd(&(bar)[XB_TMO], 1u); break; } } } } while (0)
; __device__ __forceinline__ void xcd_barrier(const XcdBarrier& b) {
;     ...
;         unsigned nloc = b.st[0], nx = b.st[1];
;         if (nloc == 0u) { xcd_barrier_complete(bar, b.x, nloc, nx); b.st[0] = nloc; b.st[1] = nx; }
;         const unsigned old = xb_add(&bar[XB_XSUB(b.x)], 1u);
;         const unsigned gen = old / nloc;
;         if (old + 1u == (gen + 1u) * nloc) {
;             __builtin_amdgcn_fence(__ATOMIC_RELEASE, "agent");
;             asm volatile("s_waitcnt vmcnt(0)" ::: "memory");
;             const unsigned og = xb_add(&bar[XB_TOP], 1u);
;             const unsigned tg = og / nx;
;             if (og + 1u == (tg + 1u) * nx) xb_add(&bar[XB_TOPGEN], 1u);
;             else XB_SPIN(xb_ld(&bar[XB_TOPGEN]) == tg, bar);
;             __builtin_amdgcn_fence(__ATOMIC_ACQUIRE, "agent");
;             xb_add(&bar[XB_XGEN(b.x)], 1u);
;             asm volatile("s_waitcnt vmcnt(0)" ::: "memory");
;         } else {
;             XB_SPIN(xb_ld(&bar[XB_XGEN(b.x)]) == gen, bar);
;             __builtin_amdgcn_fence(__ATOMIC_ACQUIRE, "agent");
;             asm volatile("s_waitcnt vmcnt(0)" ::: "memory");
.LBB0_4558:
	v_readlane_b32 s0, v255, 37
	v_readlane_b32 s1, v255, 38
	v_cvt_f32_u32_e32 v3, v4
	v_sub_u32_e32 v6, 0, v4
	v_rcp_iflag_f32_e32 v3, v3
	s_nop 1
	global_atomic_add v5, v133, v171, s[0:1] sc0
	buffer_inv sc1
	v_mul_f32_e32 v3, 0x4f7ffffe, v3
	v_cvt_u32_f32_e32 v3, v3
	v_mul_lo_u32 v6, v6, v3
	v_mul_hi_u32 v6, v3, v6
	v_add_u32_e32 v3, v3, v6
	s_waitcnt vmcnt(1)
	v_mul_hi_u32 v3, v5, v3
	v_mul_lo_u32 v6, v3, v4
	v_sub_u32_e32 v6, v5, v6
	v_add_u32_e32 v7, 1, v3
	v_cmp_ge_u32_e32 vcc, v6, v4
	v_add_u32_e32 v5, 1, v5
	s_nop 0
	v_cndmask_b32_e32 v3, v3, v7, vcc
	v_sub_u32_e32 v7, v6, v4
	v_cndmask_b32_e32 v6, v6, v7, vcc
	v_add_u32_e32 v7, 1, v3
	v_cmp_ge_u32_e32 vcc, v6, v4
	s_nop 1
	v_cndmask_b32_e32 v3, v3, v7, vcc
	v_mul_lo_u32 v6, v4, v3
	v_add_u32_e32 v4, v6, v4
	v_cmp_ne_u32_e32 vcc, v5, v4
	s_and_saveexec_b64 s[0:1], vcc
	s_xor_b64 s[22:23], exec, s[0:1]
	s_cbranch_execz .LBB0_4572
	v_readlane_b32 s0, v253, 8
	v_readlane_b32 s1, v253, 9
	s_waitcnt lgkmcnt(0)
	s_nop 3
	global_load_dword v2, v133, s[0:1] sc1
	s_waitcnt vmcnt(0)
	v_cmp_eq_u32_e32 vcc, v2, v3
	s_and_saveexec_b64 s[38:39], vcc
	s_cbranch_execz .LBB0_4571
	s_mov_b32 s0, 1
	s_mov_b64 s[40:41], 0
	s_branch .LBB0_4562
